# baseline (speedup 1.0000x reference)
.Lkc_skip_b:
	s_add_i32 s27, s27, 2
	s_cmp_gt_u32 s27, 10
	s_cselect_b32 s60, s66, s67
	s_cselect_b32 s59, s66, s68
	v_max3_f32 v156, v112, v113, v48
	v_max3_f32 v157, v114, v115, v49
	s_nop 0
	v_max3_f32 v156, v156, v50, v51
	v_mfma_f32_32x32x16_bf16 a[16:31], v[172:175], v[144:147], a[16:31]
	ds_read_b128 a[224:227], v218 offset:8192
	v_max3_f32 v156, v156, v116, v117
	v_max3_f32 v157, v157, v118, v119
	v_max3_f32 v156, v156, v52, v53
	v_max3_f32 v157, v157, v54, v55
	v_mfma_f32_32x32x16_bf16 a[32:47], v[164:167], v[128:131], a[32:47]
	ds_read_b128 a[228:231], v219 offset:8192
	v_max3_f32 v156, v156, v120, v121
	v_max3_f32 v157, v157, v122, v123
	v_max3_f32 v156, v156, v56, v57
	v_max3_f32 v157, v157, v58, v59
	v_mfma_f32_32x32x16_bf16 a[48:63], v[164:167], v[144:147], a[48:63]
	ds_read_b128 a[232:235], v220 offset:8192
	v_max3_f32 v156, v156, v124, v125
	v_max3_f32 v157, v157, v126, v127
	v_max3_f32 v156, v156, v60, v61
	v_max3_f32 v157, v157, v62, v63
	v_mfma_f32_32x32x16_bf16 a[64:79], v[160:163], v[128:131], a[64:79]
	ds_read_b128 a[236:239], v221 offset:8192
	v_max3_f32 v158, v96, v97, v32
	v_max3_f32 v159, v98, v99, v33
	v_max3_f32 v158, v158, v34, v35
	v_mfma_f32_32x32x16_bf16 a[80:95], v[160:163], v[144:147], a[80:95]
	ds_read_b128 a[240:243], v218 offset:8320
	v_max3_f32 v158, v158, v100, v101
	v_max3_f32 v159, v159, v102, v103
	v_max3_f32 v158, v158, v36, v37
	v_max3_f32 v159, v159, v38, v39
	v_mfma_f32_32x32x16_bf16 a[96:111], v[136:139], v[128:131], a[96:111]
	ds_read_b128 a[244:247], v219 offset:8320
	v_max3_f32 v128, v158, v104, v105
	v_max3_f32 v129, v159, v106, v107
	v_max3_f32 v128, v128, v40, v41
	v_max3_f32 v129, v129, v42, v43
	v_mfma_f32_32x32x16_bf16 a[112:127], v[136:139], v[144:147], a[112:127]
	ds_read_b128 a[248:251], v220 offset:8320
	v_max3_f32 v128, v128, v108, v109
	v_max3_f32 v129, v129, v110, v111
	v_max3_f32 v128, v128, v44, v45
	v_max3_f32 v130, v129, v46, v47
	v_mfma_f32_32x32x16_bf16 a[0:15], v[132:135], v[84:87], a[0:15]
	ds_read_b128 a[252:255], v221 offset:8320
	v_max_f32_e32 v129, v156, v157
	v_mov_b32_e32 v131, v129
	s_nop 1
	v_permlane32_swap_b32_e32 v129, v131
	v_max_f32_e32 v129, v129, v131
	v_mfma_f32_32x32x16_bf16 a[16:31], v[132:135], v[140:143], a[16:31]
	v_max_f32_e32 v128, v128, v130
	v_mov_b32_e32 v130, v128
	s_nop 1
	v_permlane32_swap_b32_e32 v128, v130
	v_max_f32_e32 v128, v128, v130
	v_max_f32_e32 v130, v129, v129
	v_max_f32_e32 v131, v128, v128
	v_max_f32_e32 v130, v130, v131
	v_mfma_f32_32x32x16_bf16 a[32:47], v[92:95], v[84:87], a[32:47]
	v_cmp_lt_f32_e32 vcc, s31, v130
	s_cmp_lg_u64 vcc, 0
	s_cselect_b64 s[0:1], -1, 0
	s_cbranch_vccnz .LBB0_24

.LBB0_21:
	s_waitcnt lgkmcnt(0)
	s_bitcmp1_b32 s71, s27
	s_cbranch_scc1 .Ltail_events
